# combine phase: the 16 per-expert slot lookups of a row are loaded by one per-lane load and read back with v_readlane instead of 16 dependent uniform loads
# speedup vs baseline: 1.0115x; 1.0115x over previous
.LBB0_2205:
	v_mov_b32_e32 v4, v2
	v_mov_b32_e32 v5, v2
	v_mov_b32_e32 v6, v2
	v_mov_b32_e32 v7, v2
	v_mov_b32_e32 v8, v2
	v_mov_b32_e32 v9, v2
	s_waitcnt vmcnt(9)
	v_mov_b32_e32 v10, v2
	v_mov_b32_e32 v11, v2
	v_mov_b32_e32 v12, v2
	v_mov_b32_e32 v13, v2
	s_waitcnt vmcnt(8)
	v_mov_b32_e32 v14, v2
	v_mov_b32_e32 v15, v2
	v_mov_b32_e32 v16, v2
	v_mov_b32_e32 v17, v2
	s_waitcnt vmcnt(7)
	v_mov_b32_e32 v18, v2
	v_mov_b32_e32 v19, v2
	v_mov_b32_e32 v20, v2
	v_mov_b32_e32 v21, v2
	s_waitcnt vmcnt(6)
	v_mov_b32_e32 v22, v2
	v_mov_b32_e32 v23, v2
	v_mov_b32_e32 v24, v2
	v_mov_b32_e32 v25, v2
	s_waitcnt vmcnt(5)
	v_mov_b32_e32 v26, v2
	v_mov_b32_e32 v27, v2
	v_mov_b32_e32 v28, v2
	v_mov_b32_e32 v29, v2
	s_waitcnt vmcnt(4)
	v_mov_b32_e32 v30, v2
	v_mov_b32_e32 v31, v2
	v_mov_b32_e32 v32, v2
	v_mov_b32_e32 v33, v2
	v_mov_b32_e32 v3, v2
	v_mov_b64_e32 v[34:35], v[32:33]
	s_mov_b64 s[16:17], 0
	s_mov_b64 s[18:19], s[10:11]
	v_mov_b64_e32 v[32:33], v[30:31]
	v_mov_b64_e32 v[30:31], v[28:29]
	v_mov_b64_e32 v[28:29], v[26:27]
	v_mov_b64_e32 v[26:27], v[24:25]
	v_mov_b64_e32 v[24:25], v[22:23]
	v_mov_b64_e32 v[22:23], v[20:21]
	v_mov_b64_e32 v[20:21], v[18:19]
	v_mov_b64_e32 v[18:19], v[16:17]
	v_mov_b64_e32 v[16:17], v[14:15]
	v_mov_b64_e32 v[14:15], v[12:13]
	v_mov_b64_e32 v[12:13], v[10:11]
	v_mov_b64_e32 v[10:11], v[8:9]
	v_mov_b64_e32 v[8:9], v[6:7]
	v_mov_b64_e32 v[6:7], v[4:5]
	v_mov_b64_e32 v[4:5], v[2:3]
	v_mbcnt_lo_u32_b32 v101, -1, 0
	v_mbcnt_hi_u32_b32 v101, -1, v101
	v_and_b32_e32 v101, 15, v101
	v_mul_u32_u24_e32 v101, 0x10400, v101
	global_load_dword v100, v101, s[18:19]
	s_waitcnt vmcnt(0)
	s_branch .LBB0_2207

.LBB0_2207:
	s_mul_hi_u32 s5, s16, 0x1c71c8
	s_nop 3
	v_readlane_b32 s5, v100, s5
	s_nop 1
	v_mov_b32_e32 v3, s5
	s_nop 0
	v_cmp_gt_i32_e32 vcc, 0, v3
	v_readfirstlane_b32 s5, v3
	s_cbranch_vccnz .LBB0_2206
	s_add_u32 s30, s16, s5
	s_addc_u32 s31, s17, 0
	s_lshl_b64 s[34:35], s[30:31], 2
	s_add_u32 s34, s20, s34
	s_addc_u32 s35, s21, s35
	s_lshl_b64 s[30:31], s[30:31], 12
	v_lshl_add_u64 v[36:37], v[48:49], 0, s[30:31]
	global_load_dwordx2 v[38:39], v[36:37], off
	global_load_dwordx2 v[40:41], v[36:37], off offset:512
	global_load_dwordx2 v[42:43], v[36:37], off offset:1024
	global_load_dwordx2 v[44:45], v[36:37], off offset:1536
	global_load_dwordx2 v[46:47], v[36:37], off offset:2048
	global_load_dwordx2 v[76:77], v[36:37], off offset:2560
	global_load_dwordx2 v[78:79], v[36:37], off offset:3072
	s_nop 0
	global_load_dwordx2 v[36:37], v[36:37], off offset:3584
	s_nop 0
	global_load_dword v80, v2, s[34:35]
	s_waitcnt vmcnt(8)
	v_lshlrev_b32_e32 v82, 16, v38
	v_and_b32_e32 v83, 0xffff0000, v38
	v_lshlrev_b32_e32 v38, 16, v39
	v_and_b32_e32 v39, 0xffff0000, v39
	s_waitcnt vmcnt(7)
	v_lshlrev_b32_e32 v84, 16, v40
	v_and_b32_e32 v85, 0xffff0000, v40
	v_lshlrev_b32_e32 v40, 16, v41
	v_and_b32_e32 v41, 0xffff0000, v41
	s_waitcnt vmcnt(6)
	v_lshlrev_b32_e32 v86, 16, v42
	v_and_b32_e32 v87, 0xffff0000, v42
	v_lshlrev_b32_e32 v42, 16, v43
	v_and_b32_e32 v43, 0xffff0000, v43
	s_waitcnt vmcnt(5)
	v_lshlrev_b32_e32 v88, 16, v44
	v_and_b32_e32 v89, 0xffff0000, v44
	v_lshlrev_b32_e32 v44, 16, v45
	v_and_b32_e32 v45, 0xffff0000, v45
	s_waitcnt vmcnt(4)
	v_lshlrev_b32_e32 v90, 16, v46
	v_and_b32_e32 v91, 0xffff0000, v46
	v_lshlrev_b32_e32 v46, 16, v47
	v_and_b32_e32 v47, 0xffff0000, v47
	s_waitcnt vmcnt(3)
	v_lshlrev_b32_e32 v92, 16, v76
	v_and_b32_e32 v93, 0xffff0000, v76
	v_lshlrev_b32_e32 v76, 16, v77
	v_and_b32_e32 v77, 0xffff0000, v77
	s_waitcnt vmcnt(2)
	v_lshlrev_b32_e32 v94, 16, v78
	v_and_b32_e32 v95, 0xffff0000, v78
	v_lshlrev_b32_e32 v78, 16, v79
	v_and_b32_e32 v79, 0xffff0000, v79
	s_waitcnt vmcnt(1)
	v_lshlrev_b32_e32 v96, 16, v36
	v_and_b32_e32 v97, 0xffff0000, v36
	v_lshlrev_b32_e32 v36, 16, v37
	v_and_b32_e32 v37, 0xffff0000, v37
	s_waitcnt vmcnt(0)
	v_pk_fma_f32 v[34:35], v[80:81], v[36:37], v[34:35] op_sel_hi:[0,1,1]
	v_pk_fma_f32 v[32:33], v[80:81], v[96:97], v[32:33] op_sel_hi:[0,1,1]
	v_pk_fma_f32 v[30:31], v[80:81], v[78:79], v[30:31] op_sel_hi:[0,1,1]
	v_pk_fma_f32 v[28:29], v[80:81], v[94:95], v[28:29] op_sel_hi:[0,1,1]
	v_pk_fma_f32 v[26:27], v[80:81], v[76:77], v[26:27] op_sel_hi:[0,1,1]
	v_pk_fma_f32 v[24:25], v[80:81], v[92:93], v[24:25] op_sel_hi:[0,1,1]
	v_pk_fma_f32 v[22:23], v[80:81], v[46:47], v[22:23] op_sel_hi:[0,1,1]
	v_pk_fma_f32 v[20:21], v[80:81], v[90:91], v[20:21] op_sel_hi:[0,1,1]
	v_pk_fma_f32 v[18:19], v[80:81], v[44:45], v[18:19] op_sel_hi:[0,1,1]
	v_pk_fma_f32 v[16:17], v[80:81], v[88:89], v[16:17] op_sel_hi:[0,1,1]
	v_pk_fma_f32 v[14:15], v[80:81], v[42:43], v[14:15] op_sel_hi:[0,1,1]
	v_pk_fma_f32 v[12:13], v[80:81], v[86:87], v[12:13] op_sel_hi:[0,1,1]
	v_pk_fma_f32 v[10:11], v[80:81], v[40:41], v[10:11] op_sel_hi:[0,1,1]
	v_pk_fma_f32 v[8:9], v[80:81], v[84:85], v[8:9] op_sel_hi:[0,1,1]
	v_pk_fma_f32 v[6:7], v[80:81], v[38:39], v[6:7] op_sel_hi:[0,1,1]
	v_pk_fma_f32 v[4:5], v[80:81], v[82:83], v[4:5] op_sel_hi:[0,1,1]
	s_branch .LBB0_2206

.LBB0_4009:
	s_nop 0
	v_mov_b32_e32 v2, v0
	v_mov_b32_e32 v3, v0
	v_mov_b32_e32 v4, v0
	v_mov_b32_e32 v5, v0
	s_waitcnt vmcnt(4)
	v_mov_b32_e32 v6, v0
	v_mov_b32_e32 v7, v0
	v_mov_b32_e32 v8, v0
	v_mov_b32_e32 v9, v0
	v_mov_b32_e32 v10, v0
	v_mov_b32_e32 v11, v0
	v_mov_b32_e32 v12, v0
	v_mov_b32_e32 v13, v0
	v_mov_b32_e32 v14, v0
	v_mov_b32_e32 v15, v0
	v_mov_b32_e32 v16, v0
	v_mov_b32_e32 v17, v0
	v_mov_b32_e32 v18, v0
	v_mov_b32_e32 v19, v0
	v_mov_b32_e32 v20, v0
	v_mov_b32_e32 v21, v0
	v_mov_b32_e32 v22, v0
	v_mov_b32_e32 v23, v0
	v_mov_b32_e32 v24, v0
	v_mov_b32_e32 v25, v0
	v_mov_b32_e32 v26, v0
	v_mov_b32_e32 v27, v0
	v_mov_b32_e32 v28, v0
	v_mov_b32_e32 v29, v0
	v_mov_b32_e32 v30, v0
	v_mov_b32_e32 v31, v0
	v_mov_b32_e32 v1, v0
	v_mov_b64_e32 v[32:33], v[30:31]
	s_mov_b64 s[10:11], 0
	s_mov_b64 s[12:13], s[6:7]
	v_mov_b64_e32 v[30:31], v[28:29]
	v_mov_b64_e32 v[28:29], v[26:27]
	v_mov_b64_e32 v[26:27], v[24:25]
	v_mov_b64_e32 v[24:25], v[22:23]
	v_mov_b64_e32 v[22:23], v[20:21]
	v_mov_b64_e32 v[20:21], v[18:19]
	v_mov_b64_e32 v[18:19], v[16:17]
	v_mov_b64_e32 v[16:17], v[14:15]
	v_mov_b64_e32 v[14:15], v[12:13]
	v_mov_b64_e32 v[12:13], v[10:11]
	v_mov_b64_e32 v[10:11], v[8:9]
	v_mov_b64_e32 v[8:9], v[6:7]
	v_mov_b64_e32 v[6:7], v[4:5]
	v_mov_b64_e32 v[4:5], v[2:3]
	v_mov_b64_e32 v[2:3], v[0:1]
	v_mbcnt_lo_u32_b32 v101, -1, 0
	v_mbcnt_hi_u32_b32 v101, -1, v101
	v_and_b32_e32 v101, 15, v101
	v_mul_u32_u24_e32 v101, 0x10400, v101
	global_load_dword v100, v101, s[12:13]
	s_waitcnt vmcnt(0)
	s_branch .LBB0_4011

.LBB0_4011:
	s_mul_hi_u32 s1, s10, 0x1c71c8
	s_nop 3
	v_readlane_b32 s1, v100, s1
	s_nop 1
	v_mov_b32_e32 v1, s1
	s_nop 0
	v_cmp_gt_i32_e32 vcc, 0, v1
	v_readfirstlane_b32 s1, v1
	s_cbranch_vccnz .LBB0_4010
	s_add_u32 s16, s10, s1
	s_addc_u32 s17, s11, 0
	s_lshl_b64 s[18:19], s[16:17], 2
	s_add_u32 s18, s14, s18
	s_addc_u32 s19, s15, s19
	s_lshl_b64 s[16:17], s[16:17], 12
	v_lshl_add_u64 v[50:51], v[34:35], 0, s[16:17]
	global_load_dwordx2 v[52:53], v[50:51], off
	global_load_dwordx2 v[54:55], v[50:51], off offset:512
	global_load_dwordx2 v[56:57], v[50:51], off offset:1024
	global_load_dwordx2 v[58:59], v[50:51], off offset:1536
	global_load_dwordx2 v[60:61], v[50:51], off offset:2048
	global_load_dwordx2 v[62:63], v[50:51], off offset:2560
	global_load_dwordx2 v[64:65], v[50:51], off offset:3072
	global_load_dwordx2 v[66:67], v[50:51], off offset:3584
	global_load_dword v68, v0, s[18:19]
	s_waitcnt vmcnt(8)
	v_lshlrev_b32_e32 v50, 16, v52
	v_and_b32_e32 v51, 0xffff0000, v52
	v_lshlrev_b32_e32 v52, 16, v53
	v_and_b32_e32 v53, 0xffff0000, v53
	s_waitcnt vmcnt(7)
	v_lshlrev_b32_e32 v70, 16, v54
	v_and_b32_e32 v71, 0xffff0000, v54
	v_lshlrev_b32_e32 v54, 16, v55
	v_and_b32_e32 v55, 0xffff0000, v55
	s_waitcnt vmcnt(6)
	v_lshlrev_b32_e32 v72, 16, v56
	v_and_b32_e32 v73, 0xffff0000, v56
	v_lshlrev_b32_e32 v56, 16, v57
	v_and_b32_e32 v57, 0xffff0000, v57
	s_waitcnt vmcnt(5)
	v_lshlrev_b32_e32 v74, 16, v58
	v_and_b32_e32 v75, 0xffff0000, v58
	v_lshlrev_b32_e32 v58, 16, v59
	v_and_b32_e32 v59, 0xffff0000, v59
	s_waitcnt vmcnt(4)
	v_lshlrev_b32_e32 v76, 16, v60
	v_and_b32_e32 v77, 0xffff0000, v60
	v_lshlrev_b32_e32 v60, 16, v61
	v_and_b32_e32 v61, 0xffff0000, v61
	s_waitcnt vmcnt(3)
	v_lshlrev_b32_e32 v78, 16, v62
	v_and_b32_e32 v79, 0xffff0000, v62
	v_lshlrev_b32_e32 v62, 16, v63
	v_and_b32_e32 v63, 0xffff0000, v63
	s_waitcnt vmcnt(2)
	v_lshlrev_b32_e32 v80, 16, v64
	v_and_b32_e32 v81, 0xffff0000, v64
	v_lshlrev_b32_e32 v64, 16, v65
	v_and_b32_e32 v65, 0xffff0000, v65
	s_waitcnt vmcnt(1)
	v_lshlrev_b32_e32 v82, 16, v66
	v_and_b32_e32 v83, 0xffff0000, v66
	v_lshlrev_b32_e32 v66, 16, v67
	v_and_b32_e32 v67, 0xffff0000, v67
	s_waitcnt vmcnt(0)
	v_pk_fma_f32 v[32:33], v[68:69], v[66:67], v[32:33] op_sel_hi:[0,1,1]
	v_pk_fma_f32 v[30:31], v[68:69], v[82:83], v[30:31] op_sel_hi:[0,1,1]
	v_pk_fma_f32 v[28:29], v[68:69], v[64:65], v[28:29] op_sel_hi:[0,1,1]
	v_pk_fma_f32 v[26:27], v[68:69], v[80:81], v[26:27] op_sel_hi:[0,1,1]
	v_pk_fma_f32 v[24:25], v[68:69], v[62:63], v[24:25] op_sel_hi:[0,1,1]
	v_pk_fma_f32 v[22:23], v[68:69], v[78:79], v[22:23] op_sel_hi:[0,1,1]
	v_pk_fma_f32 v[20:21], v[68:69], v[60:61], v[20:21] op_sel_hi:[0,1,1]
	v_pk_fma_f32 v[18:19], v[68:69], v[76:77], v[18:19] op_sel_hi:[0,1,1]
	v_pk_fma_f32 v[16:17], v[68:69], v[58:59], v[16:17] op_sel_hi:[0,1,1]
	v_pk_fma_f32 v[14:15], v[68:69], v[74:75], v[14:15] op_sel_hi:[0,1,1]
	v_pk_fma_f32 v[12:13], v[68:69], v[56:57], v[12:13] op_sel_hi:[0,1,1]
	v_pk_fma_f32 v[10:11], v[68:69], v[72:73], v[10:11] op_sel_hi:[0,1,1]
	v_pk_fma_f32 v[8:9], v[68:69], v[54:55], v[8:9] op_sel_hi:[0,1,1]
	v_pk_fma_f32 v[6:7], v[68:69], v[70:71], v[6:7] op_sel_hi:[0,1,1]
	v_pk_fma_f32 v[4:5], v[68:69], v[52:53], v[4:5] op_sel_hi:[0,1,1]
	v_pk_fma_f32 v[2:3], v[68:69], v[50:51], v[2:3] op_sel_hi:[0,1,1]
	s_branch .LBB0_4010
